# attention tile loops: any-need test via scalar mask algebra + SCC branch (no EXEC save/restore, no re-derived ballot); first V-read group hoisted to the softmax block head
# speedup vs baseline: 1.0048x; 1.0048x over previous
.LBB0_395:
	v_add_u32_e32 v147, s88, v149
	v_mov_b32_e32 v109, v180
	v_add_u32_e32 v180, v147, v151
	ds_read_b128 v[188:191], v180 offset:0
	v_mov_b32_e32 v110, v181
	v_add_u32_e32 v181, v147, v182
	ds_read_b128 v[218:221], v181 offset:0
	v_add_u32_e32 v187, v147, v183
	ds_read_b128 v[222:225], v187 offset:0
	s_waitcnt lgkmcnt(2)
	v_add_u32_e32 v147, v147, v184
	v_mfma_f32_16x16x32_bf16 v[108:111], v[188:191], v[38:41], v[108:111]
	v_mfma_f32_16x16x32_bf16 v[112:115], v[188:191], v[54:57], v[112:115]
	ds_read_b128 v[188:191], v147 offset:0
	s_waitcnt lgkmcnt(2)
	v_mfma_f32_16x16x32_bf16 v[108:111], v[218:221], v[42:45], v[108:111]
	v_mfma_f32_16x16x32_bf16 v[112:115], v[218:221], v[58:61], v[112:115]
	ds_read_b128 v[218:221], v180 offset:0x1000
	s_waitcnt lgkmcnt(2)
	v_mfma_f32_16x16x32_bf16 v[108:111], v[222:225], v[46:49], v[108:111]
	ds_read_b128 v[226:229], v181 offset:0x1000
	s_waitcnt lgkmcnt(2)
	v_mfma_f32_16x16x32_bf16 v[222:225], v[222:225], v[62:65], v[112:115]
	v_mfma_f32_16x16x32_bf16 v[112:115], v[188:191], v[50:53], v[108:111]
	v_mfma_f32_16x16x32_bf16 v[108:111], v[188:191], v[66:69], v[222:225]
	ds_read_b128 v[188:191], v187 offset:0x1000
	s_waitcnt lgkmcnt(2)
	v_mfma_f32_16x16x32_bf16 v[116:119], v[218:221], v[38:41], v[116:119]
	v_mfma_f32_16x16x32_bf16 v[120:123], v[218:221], v[54:57], v[120:123]
	ds_read_b128 v[218:221], v147 offset:0x1000
	s_waitcnt lgkmcnt(2)
	v_mfma_f32_16x16x32_bf16 v[116:119], v[226:229], v[42:45], v[116:119]
	ds_read_b128 v[222:225], v180 offset:0x2000
	s_waitcnt lgkmcnt(2)
	v_mfma_f32_16x16x32_bf16 v[120:123], v[226:229], v[58:61], v[120:123]
	v_mfma_f32_16x16x32_bf16 v[116:119], v[188:191], v[46:49], v[116:119]
	ds_read_b128 v[226:229], v181 offset:0x2000
	s_waitcnt lgkmcnt(2)
	v_mfma_f32_16x16x32_bf16 v[188:191], v[188:191], v[62:65], v[120:123]
	v_mfma_f32_16x16x32_bf16 v[120:123], v[218:221], v[50:53], v[116:119]
	v_mfma_f32_16x16x32_bf16 v[116:119], v[218:221], v[66:69], v[188:191]
	ds_read_b128 v[188:191], v187 offset:0x2000
	s_waitcnt lgkmcnt(2)
	v_mfma_f32_16x16x32_bf16 v[124:127], v[222:225], v[38:41], v[124:127]
	ds_read_b128 v[218:221], v147 offset:0x2000
	s_waitcnt lgkmcnt(2)
	v_mfma_f32_16x16x32_bf16 v[132:135], v[222:225], v[54:57], v[132:135]
	v_mfma_f32_16x16x32_bf16 v[124:127], v[226:229], v[42:45], v[124:127]
	ds_read_b128 v[222:225], v180 offset:0x3000
	s_waitcnt lgkmcnt(2)
	v_mfma_f32_16x16x32_bf16 v[132:135], v[226:229], v[58:61], v[132:135]
	s_nop 1
	v_mfma_f32_16x16x32_bf16 v[124:127], v[188:191], v[46:49], v[124:127]
	ds_read_b128 v[226:229], v181 offset:0x3000
	s_waitcnt lgkmcnt(2)
	v_mfma_f32_16x16x32_bf16 v[188:191], v[188:191], v[62:65], v[132:135]
	v_mfma_f32_16x16x32_bf16 v[132:135], v[218:221], v[50:53], v[124:127]
	v_mfma_f32_16x16x32_bf16 v[124:127], v[218:221], v[66:69], v[188:191]
	ds_read_b128 v[188:191], v187 offset:0x3000
	s_waitcnt lgkmcnt(2)
	v_mfma_f32_16x16x32_bf16 v[128:131], v[222:225], v[38:41], v[128:131]
	ds_read_b128 v[218:221], v147 offset:0x3000
	s_waitcnt lgkmcnt(2)
	v_mfma_f32_16x16x32_bf16 v[136:139], v[222:225], v[54:57], v[136:139]
	v_mfma_f32_16x16x32_bf16 v[128:131], v[226:229], v[42:45], v[128:131]
	s_waitcnt lgkmcnt(1)
	v_mfma_f32_16x16x32_bf16 v[136:139], v[226:229], v[58:61], v[136:139]
	s_nop 1
	v_mfma_f32_16x16x32_bf16 v[128:131], v[188:191], v[46:49], v[128:131]
	s_waitcnt lgkmcnt(0)
	v_mfma_f32_16x16x32_bf16 v[188:191], v[188:191], v[62:65], v[136:139]
	v_and_b32_e32 v180, 64, v208
	v_xor_b32_e32 v147, 16, v208
	v_add_u32_e32 v180, 64, v180
	v_cmp_lt_i32_e32 vcc, v147, v180
	v_mfma_f32_16x16x32_bf16 v[136:139], v[218:221], v[50:53], v[128:131]
	s_mov_b64 s[0:1], 0
	v_cndmask_b32_e32 v147, v208, v147, vcc
	v_lshlrev_b32_e32 v181, 2, v147
	v_xor_b32_e32 v147, 32, v208
	v_cmp_lt_i32_e32 vcc, v147, v180
	v_mfma_f32_16x16x32_bf16 v[128:131], v[218:221], v[66:69], v[188:191]
	s_mov_b64 s[54:55], 0
	v_cndmask_b32_e32 v147, v208, v147, vcc
	v_lshlrev_b32_e32 v187, 2, v147
	v_max3_f32 v147, v112, s30, v113
	v_max3_f32 v147, v147, v114, v115
	v_max3_f32 v147, v147, v120, v121
	v_max3_f32 v147, v147, v122, v123
	v_max3_f32 v147, v147, v132, v133
	v_max3_f32 v147, v147, v134, v135
	v_max3_f32 v147, v147, v136, v137
	v_max3_f32 v147, v147, v138, v139
	v_max3_f32 v180, v108, s30, v109
	v_max3_f32 v180, v180, v110, v111
	v_max3_f32 v180, v180, v116, v117
	v_max3_f32 v180, v180, v118, v119
	v_max3_f32 v180, v180, v124, v125
	v_max3_f32 v180, v180, v126, v127
	v_max3_f32 v180, v180, v128, v129
	v_max3_f32 v180, v180, v130, v131
	v_mov_b32_e32 v230, v147
	v_mov_b32_e32 v231, v180
	s_nop 1
	v_permlane16_swap_b32 v230, v147
	v_permlane16_swap_b32 v231, v180
	v_max_f32_e32 v147, v147, v230
	v_max_f32_e32 v180, v180, v231
	v_mov_b32_e32 v230, v147
	v_mov_b32_e32 v231, v180
	s_nop 1
	v_permlane32_swap_b32 v230, v147
	v_permlane32_swap_b32 v231, v180
	v_max_f32_e32 v147, v147, v230
	v_max_f32_e32 v180, v180, v231
	v_cmp_lt_f32_e64 s[56:57], s31, v147
	v_cmp_lt_f32_e32 vcc, s34, v147
	s_orn2_b64 s[54:55], vcc, s[52:53]
	s_and_b64 s[54:55], s[54:55], s[56:57]
	v_cmp_lt_f32_e64 s[56:57], s31, v180
	v_cmp_lt_f32_e32 vcc, s34, v180
	s_orn2_b64 s[0:1], vcc, s[48:49]
	s_and_b64 s[0:1], s[0:1], s[56:57]
	s_or_b64 s[56:57], s[54:55], s[0:1]
	s_cbranch_scc0 .LBB0_401
	v_cndmask_b32_e64 v188, 0, v180, s[0:1]
	v_cndmask_b32_e64 v147, 0, v147, s[54:55]
	v_exp_f32_e64 v180, -v188
	v_exp_f32_e64 v187, -v147
	s_and_b64 vcc, s[0:1], s[48:49]
	s_or_b64 s[0:1], s[48:49], s[0:1]
	v_cndmask_b32_e32 v181, 1.0, v180, vcc
	s_and_b64 vcc, s[54:55], s[52:53]
	v_cndmask_b32_e32 v180, 1.0, v187, vcc
	s_or_b64 s[54:55], s[52:53], s[54:55]
	v_pk_mul_f32 v[100:101], v[100:101], v[180:181] op_sel_hi:[1,0]
	v_pk_mul_f32 v[98:99], v[98:99], v[180:181] op_sel_hi:[1,0]
	v_pk_mul_f32 v[96:97], v[96:97], v[180:181] op_sel_hi:[1,0]
	v_pk_mul_f32 v[94:95], v[94:95], v[180:181] op_sel_hi:[1,0]
	v_pk_mul_f32 v[92:93], v[92:93], v[180:181] op_sel_hi:[1,0]
	v_pk_mul_f32 v[90:91], v[90:91], v[180:181] op_sel_hi:[1,0]
	v_pk_mul_f32 v[88:89], v[88:89], v[180:181] op_sel_hi:[1,0]
	v_pk_mul_f32 v[86:87], v[86:87], v[180:181] op_sel_hi:[1,0]
	v_pk_mul_f32 v[84:85], v[84:85], v[180:181] op_sel_hi:[1,0]
	v_pk_mul_f32 v[82:83], v[82:83], v[180:181] op_sel_hi:[1,0]
	v_pk_mul_f32 v[80:81], v[80:81], v[180:181] op_sel_hi:[1,0]
	v_pk_mul_f32 v[78:79], v[78:79], v[180:181] op_sel_hi:[1,0]
	v_pk_mul_f32 v[76:77], v[76:77], v[180:181] op_sel_hi:[1,0]
	v_pk_mul_f32 v[74:75], v[74:75], v[180:181] op_sel_hi:[1,0]
	v_pk_mul_f32 v[72:73], v[72:73], v[180:181] op_sel_hi:[1,0]
	v_pk_mul_f32 v[70:71], v[70:71], v[180:181] op_sel_hi:[1,0]
	v_pk_mul_f32 v[152:153], v[152:153], v[180:181]
	v_mov_b32_e32 v180, v181
	s_andn2_b64 s[52:53], s[52:53], exec
	s_and_b64 s[54:55], s[54:55], exec
	s_andn2_b64 s[48:49], s[48:49], exec
	s_and_b64 s[0:1], s[0:1], exec
	v_add_f32_e32 v146, v146, v147
	v_sub_f32_e32 v112, v112, v147
	v_sub_f32_e32 v113, v113, v147
	v_sub_f32_e32 v114, v114, v147
	v_sub_f32_e32 v115, v115, v147
	v_sub_f32_e32 v120, v120, v147
	v_sub_f32_e32 v121, v121, v147
	v_sub_f32_e32 v122, v122, v147
	v_sub_f32_e32 v123, v123, v147
	v_sub_f32_e32 v132, v132, v147
	v_sub_f32_e32 v133, v133, v147
	v_sub_f32_e32 v134, v134, v147
	v_sub_f32_e32 v135, v135, v147
	v_sub_f32_e32 v136, v136, v147
	v_sub_f32_e32 v137, v137, v147
	v_sub_f32_e32 v138, v138, v147
	v_sub_f32_e32 v139, v139, v147
	v_add_f32_e32 v2, v2, v188
	v_pk_mul_f32 v[36:37], v[36:37], v[180:181] op_sel_hi:[1,0]
	v_pk_mul_f32 v[34:35], v[34:35], v[180:181] op_sel_hi:[1,0]
	v_pk_mul_f32 v[32:33], v[32:33], v[180:181] op_sel_hi:[1,0]
	v_pk_mul_f32 v[30:31], v[30:31], v[180:181] op_sel_hi:[1,0]
	v_pk_mul_f32 v[28:29], v[28:29], v[180:181] op_sel_hi:[1,0]
	v_pk_mul_f32 v[26:27], v[26:27], v[180:181] op_sel_hi:[1,0]
	v_pk_mul_f32 v[20:21], v[20:21], v[180:181] op_sel_hi:[1,0]
	v_pk_mul_f32 v[18:19], v[18:19], v[180:181] op_sel_hi:[1,0]
	v_pk_mul_f32 v[24:25], v[24:25], v[180:181] op_sel_hi:[1,0]
	v_pk_mul_f32 v[22:23], v[22:23], v[180:181] op_sel_hi:[1,0]
	v_pk_mul_f32 v[16:17], v[16:17], v[180:181] op_sel_hi:[1,0]
	v_pk_mul_f32 v[14:15], v[14:15], v[180:181] op_sel_hi:[1,0]
	v_pk_mul_f32 v[12:13], v[12:13], v[180:181] op_sel_hi:[1,0]
	v_pk_mul_f32 v[10:11], v[10:11], v[180:181] op_sel_hi:[1,0]
	v_pk_mul_f32 v[8:9], v[8:9], v[180:181] op_sel_hi:[1,0]
	v_pk_mul_f32 v[6:7], v[6:7], v[180:181] op_sel_hi:[1,0]
	v_sub_f32_e32 v108, v108, v188
	v_sub_f32_e32 v109, v109, v188
	v_sub_f32_e32 v110, v110, v188
	v_sub_f32_e32 v111, v111, v188
	v_sub_f32_e32 v116, v116, v188
	v_sub_f32_e32 v117, v117, v188
	v_sub_f32_e32 v118, v118, v188
	v_sub_f32_e32 v119, v119, v188
	v_sub_f32_e32 v124, v124, v188
	v_sub_f32_e32 v125, v125, v188
	v_sub_f32_e32 v126, v126, v188
	v_sub_f32_e32 v127, v127, v188
	v_sub_f32_e32 v128, v128, v188
	v_sub_f32_e32 v129, v129, v188
	v_sub_f32_e32 v130, v130, v188
	v_sub_f32_e32 v131, v131, v188
	s_or_b64 s[52:53], s[52:53], s[54:55]
	s_or_b64 s[48:49], s[48:49], s[0:1]
.LBB0_401:
	v_add_u32_e32 v248, s88, v185
	ds_read_b64_tr_b16 v[232:233], v248 offset:0
	ds_read_b64_tr_b16 v[234:235], v248 offset:0x1000
	ds_read_b64_tr_b16 v[236:237], v248 offset:0x2000
	ds_read_b64_tr_b16 v[238:239], v248 offset:0x3000
	v_xor_b32_e32 v249, 32, v248
	ds_read_b64_tr_b16 v[240:241], v249 offset:0
	ds_read_b64_tr_b16 v[242:243], v249 offset:0x1000
	ds_read_b64_tr_b16 v[244:245], v249 offset:0x2000
	ds_read_b64_tr_b16 v[246:247], v249 offset:0x3000
	v_exp_f32_e32 v180, v112
	v_exp_f32_e32 v181, v108
	v_exp_f32_e32 v188, v113
	v_exp_f32_e32 v189, v109
	v_exp_f32_e32 v190, v114
	v_exp_f32_e32 v191, v110
	v_exp_f32_e32 v192, v115
	v_exp_f32_e32 v193, v111
	v_exp_f32_e32 v120, v120
	v_exp_f32_e32 v218, v121
	v_exp_f32_e32 v121, v116
	v_pk_add_f32 v[112:113], v[180:181], 0 op_sel_hi:[1,0]
	v_exp_f32_e32 v219, v117
	v_pk_add_f32 v[112:113], v[188:189], v[112:113]
	v_exp_f32_e32 v122, v122
	v_exp_f32_e32 v220, v123
	v_exp_f32_e32 v123, v118
	v_pk_add_f32 v[112:113], v[190:191], v[112:113]
	v_exp_f32_e32 v221, v119
	v_pk_add_f32 v[112:113], v[192:193], v[112:113]
	v_exp_f32_e32 v132, v132
	v_exp_f32_e32 v222, v133
	v_pk_add_f32 v[112:113], v[120:121], v[112:113]
	v_exp_f32_e32 v133, v124
	v_pk_add_f32 v[112:113], v[218:219], v[112:113]
	v_exp_f32_e32 v223, v125
	v_exp_f32_e32 v134, v134
	v_exp_f32_e32 v224, v135
	v_pk_add_f32 v[112:113], v[122:123], v[112:113]
	v_exp_f32_e32 v135, v126
	v_exp_f32_e32 v225, v127
	v_pk_add_f32 v[112:113], v[220:221], v[112:113]
	v_exp_f32_e32 v136, v136
	v_exp_f32_e32 v226, v137
	v_exp_f32_e32 v137, v128
	v_pk_add_f32 v[112:113], v[132:133], v[112:113]
	v_exp_f32_e32 v227, v129
	v_pk_add_f32 v[112:113], v[222:223], v[112:113]
	v_exp_f32_e32 v138, v138
	v_exp_f32_e32 v228, v139
	v_exp_f32_e32 v139, v130
	v_pk_add_f32 v[112:113], v[134:135], v[112:113]
	v_exp_f32_e32 v229, v131
	v_pk_add_f32 v[112:113], v[224:225], v[112:113]
	v_add_u32_e32 v147, s88, v185
	v_pk_add_f32 v[112:113], v[136:137], v[112:113]
	v_cvt_pk_bf16_f32 v108, v180, v188
	v_pk_add_f32 v[112:113], v[226:227], v[112:113]
	v_cvt_pk_bf16_f32 v110, v120, v218
	v_pk_add_f32 v[112:113], v[138:139], v[112:113]
	v_cvt_pk_bf16_f32 v120, v133, v223
	v_pk_add_f32 v[116:117], v[228:229], v[112:113]
	v_cvt_pk_bf16_f32 v112, v132, v222
	v_xor_b32_e32 v180, 32, v147
	v_cvt_pk_bf16_f32 v113, v134, v224
	v_cvt_pk_bf16_f32 v118, v121, v219
	v_cvt_pk_bf16_f32 v121, v135, v225
	v_cvt_pk_bf16_f32 v111, v122, v220
	v_cvt_pk_bf16_f32 v114, v136, v226
	v_cvt_pk_bf16_f32 v122, v137, v227
	v_cvt_pk_bf16_f32 v115, v138, v228
	v_cvt_pk_bf16_f32 v119, v123, v221
	v_cvt_pk_bf16_f32 v123, v139, v229
	v_pk_add_f32 v[152:153], v[152:153], v[116:117]
	v_cvt_pk_bf16_f32 v116, v181, v189
	v_xor_b32_e32 v180, 64, v147
	ds_read_b64_tr_b16 v[188:189], v180 offset:0
	v_cvt_pk_bf16_f32 v109, v190, v192
	v_cvt_pk_bf16_f32 v117, v191, v193
	ds_read_b64_tr_b16 v[190:191], v180 offset:0x1000
	ds_read_b64_tr_b16 v[218:219], v180 offset:0x2000
	ds_read_b64_tr_b16 v[220:221], v180 offset:0x3000
	v_xor_b32_e32 v180, 0x60, v147
	ds_read_b64_tr_b16 v[222:223], v180 offset:0
	ds_read_b64_tr_b16 v[224:225], v180 offset:0x1000
	ds_read_b64_tr_b16 v[226:227], v180 offset:0x2000
	ds_read_b64_tr_b16 v[228:229], v180 offset:0x3000
	s_waitcnt lgkmcnt(8)
	v_mfma_f32_16x16x32_bf16 v[98:101], v[232:235], v[108:111], v[98:101]
	v_mfma_f32_16x16x32_bf16 v[34:37], v[232:235], v[116:119], v[34:37]
	v_mfma_f32_16x16x32_bf16 v[94:97], v[240:243], v[108:111], v[94:97]
	v_mfma_f32_16x16x32_bf16 v[30:33], v[240:243], v[116:119], v[30:33]
	v_mfma_f32_16x16x32_bf16 v[98:101], v[236:239], v[112:115], v[98:101]
	v_mfma_f32_16x16x32_bf16 v[34:37], v[236:239], v[120:123], v[34:37]
	v_mfma_f32_16x16x32_bf16 v[94:97], v[244:247], v[112:115], v[94:97]
	v_mfma_f32_16x16x32_bf16 v[30:33], v[244:247], v[120:123], v[30:33]
	v_xor_b32_e32 v132, 0x80, v147
	ds_read_b64_tr_b16 v[232:233], v132 offset:0
	ds_read_b64_tr_b16 v[234:235], v132 offset:0x1000
	ds_read_b64_tr_b16 v[236:237], v132 offset:0x2000
	ds_read_b64_tr_b16 v[238:239], v132 offset:0x3000
	v_xor_b32_e32 v180, 0xa0, v147
	ds_read_b64_tr_b16 v[240:241], v180 offset:0
	ds_read_b64_tr_b16 v[242:243], v180 offset:0x1000
	ds_read_b64_tr_b16 v[244:245], v180 offset:0x2000
	ds_read_b64_tr_b16 v[246:247], v180 offset:0x3000
	s_waitcnt lgkmcnt(8)
	v_mfma_f32_16x16x32_bf16 v[90:93], v[188:191], v[108:111], v[90:93]
	v_mfma_f32_16x16x32_bf16 v[26:29], v[188:191], v[116:119], v[26:29]
	v_mfma_f32_16x16x32_bf16 v[86:89], v[222:225], v[108:111], v[86:89]
	v_mfma_f32_16x16x32_bf16 v[18:21], v[222:225], v[116:119], v[18:21]
	v_mfma_f32_16x16x32_bf16 v[90:93], v[218:221], v[112:115], v[90:93]
	v_mfma_f32_16x16x32_bf16 v[26:29], v[218:221], v[120:123], v[26:29]
	v_mfma_f32_16x16x32_bf16 v[86:89], v[226:229], v[112:115], v[86:89]
	v_mfma_f32_16x16x32_bf16 v[18:21], v[226:229], v[120:123], v[18:21]
	v_xor_b32_e32 v180, 0xc0, v147
	ds_read_b64_tr_b16 v[188:189], v180 offset:0
	ds_read_b64_tr_b16 v[190:191], v180 offset:0x1000
	ds_read_b64_tr_b16 v[218:219], v180 offset:0x2000
	ds_read_b64_tr_b16 v[220:221], v180 offset:0x3000
	v_xor_b32_e32 v147, 0xe0, v147
	ds_read_b64_tr_b16 v[222:223], v147 offset:0
	ds_read_b64_tr_b16 v[224:225], v147 offset:0x1000
	ds_read_b64_tr_b16 v[226:227], v147 offset:0x2000
	ds_read_b64_tr_b16 v[228:229], v147 offset:0x3000
	s_waitcnt lgkmcnt(8)
	v_mfma_f32_16x16x32_bf16 v[82:85], v[232:235], v[108:111], v[82:85]
	v_mfma_f32_16x16x32_bf16 v[22:25], v[232:235], v[116:119], v[22:25]
	v_mfma_f32_16x16x32_bf16 v[78:81], v[240:243], v[108:111], v[78:81]
	v_mfma_f32_16x16x32_bf16 v[14:17], v[240:243], v[116:119], v[14:17]
	v_mfma_f32_16x16x32_bf16 v[82:85], v[236:239], v[112:115], v[82:85]
	v_mfma_f32_16x16x32_bf16 v[22:25], v[236:239], v[120:123], v[22:25]
	v_mfma_f32_16x16x32_bf16 v[78:81], v[244:247], v[112:115], v[78:81]
	v_mfma_f32_16x16x32_bf16 v[14:17], v[244:247], v[120:123], v[14:17]
	s_waitcnt lgkmcnt(0)
	v_mfma_f32_16x16x32_bf16 v[74:77], v[188:191], v[108:111], v[74:77]
	v_mfma_f32_16x16x32_bf16 v[10:13], v[188:191], v[116:119], v[10:13]
	v_mfma_f32_16x16x32_bf16 v[70:73], v[222:225], v[108:111], v[70:73]
	v_mfma_f32_16x16x32_bf16 v[6:9], v[222:225], v[116:119], v[6:9]
	v_mfma_f32_16x16x32_bf16 v[74:77], v[218:221], v[112:115], v[74:77]
	v_mfma_f32_16x16x32_bf16 v[10:13], v[218:221], v[120:123], v[10:13]
	v_mfma_f32_16x16x32_bf16 v[70:73], v[226:229], v[112:115], v[70:73]
	v_mfma_f32_16x16x32_bf16 v[6:9], v[226:229], v[120:123], v[6:9]

.LBB0_413:
	v_add_u32_e32 v248, s67, v166
	ds_read_b64_tr_b16 v[232:233], v248 offset:0
	ds_read_b64_tr_b16 v[234:235], v248 offset:0x1000
	ds_read_b64_tr_b16 v[236:237], v248 offset:0x2000
	ds_read_b64_tr_b16 v[238:239], v248 offset:0x3000
	v_xor_b32_e32 v249, 32, v248
	ds_read_b64_tr_b16 v[240:241], v249 offset:0
	ds_read_b64_tr_b16 v[242:243], v249 offset:0x1000
	ds_read_b64_tr_b16 v[244:245], v249 offset:0x2000
	ds_read_b64_tr_b16 v[246:247], v249 offset:0x3000
	v_exp_f32_e32 v170, v110
	v_exp_f32_e32 v171, v106
	v_exp_f32_e32 v172, v111
	v_exp_f32_e32 v173, v107
	v_exp_f32_e32 v174, v112
	v_exp_f32_e32 v175, v108
	v_exp_f32_e32 v176, v113
	v_exp_f32_e32 v177, v109
	v_exp_f32_e32 v118, v118
	v_exp_f32_e32 v178, v119
	v_exp_f32_e32 v119, v114
	v_pk_add_f32 v[110:111], v[170:171], 0 op_sel_hi:[1,0]
	v_exp_f32_e32 v179, v115
	v_pk_add_f32 v[110:111], v[172:173], v[110:111]
	v_exp_f32_e32 v120, v120
	v_exp_f32_e32 v180, v121
	v_pk_add_f32 v[110:111], v[174:175], v[110:111]
	v_exp_f32_e32 v121, v116
	v_pk_add_f32 v[110:111], v[176:177], v[110:111]
	v_exp_f32_e32 v181, v117
	v_exp_f32_e32 v130, v130
	v_exp_f32_e32 v182, v131
	v_pk_add_f32 v[110:111], v[118:119], v[110:111]
	v_exp_f32_e32 v131, v122
	v_pk_add_f32 v[110:111], v[178:179], v[110:111]
	v_exp_f32_e32 v183, v123
	v_exp_f32_e32 v132, v132
	v_exp_f32_e32 v184, v133
	v_exp_f32_e32 v133, v124
	v_pk_add_f32 v[110:111], v[120:121], v[110:111]
	v_exp_f32_e32 v185, v125
	v_pk_add_f32 v[110:111], v[180:181], v[110:111]
	v_exp_f32_e32 v134, v134
	v_exp_f32_e32 v186, v135
	v_exp_f32_e32 v135, v126
	v_pk_add_f32 v[110:111], v[130:131], v[110:111]
	v_exp_f32_e32 v187, v127
	v_pk_add_f32 v[110:111], v[182:183], v[110:111]
	v_exp_f32_e32 v136, v136
	v_exp_f32_e32 v188, v137
	v_exp_f32_e32 v137, v128
	v_pk_add_f32 v[110:111], v[132:133], v[110:111]
	v_exp_f32_e32 v189, v129
	v_pk_add_f32 v[110:111], v[184:185], v[110:111]
	v_add_u32_e32 v158, s67, v166
	v_pk_add_f32 v[110:111], v[134:135], v[110:111]
	v_cvt_pk_bf16_f32 v108, v118, v178
	v_pk_add_f32 v[110:111], v[186:187], v[110:111]
	v_cvt_pk_bf16_f32 v118, v131, v183
	v_pk_add_f32 v[110:111], v[136:137], v[110:111]
	v_xor_b32_e32 v160, 32, v158
	v_pk_add_f32 v[114:115], v[188:189], v[110:111]
	v_cvt_pk_bf16_f32 v110, v130, v182
	v_cvt_pk_bf16_f32 v111, v132, v184
	v_cvt_pk_bf16_f32 v116, v119, v179
	v_cvt_pk_bf16_f32 v119, v133, v185
	v_cvt_pk_bf16_f32 v109, v120, v180
	v_cvt_pk_bf16_f32 v112, v134, v186
	v_cvt_pk_bf16_f32 v120, v135, v187
	v_cvt_pk_bf16_f32 v113, v136, v188
	v_cvt_pk_bf16_f32 v117, v121, v181
	v_cvt_pk_bf16_f32 v121, v137, v189
	v_cvt_pk_bf16_f32 v106, v170, v172
	v_pk_add_f32 v[144:145], v[144:145], v[114:115]
	v_cvt_pk_bf16_f32 v114, v171, v173
	v_xor_b32_e32 v160, 64, v158
	ds_read_b64_tr_b16 v[170:171], v160 offset:0
	ds_read_b64_tr_b16 v[172:173], v160 offset:0x1000
	v_cvt_pk_bf16_f32 v107, v174, v176
	v_cvt_pk_bf16_f32 v115, v175, v177
	ds_read_b64_tr_b16 v[174:175], v160 offset:0x2000
	ds_read_b64_tr_b16 v[176:177], v160 offset:0x3000
	v_xor_b32_e32 v160, 0x60, v158
	ds_read_b64_tr_b16 v[178:179], v160 offset:0
	ds_read_b64_tr_b16 v[180:181], v160 offset:0x1000
	ds_read_b64_tr_b16 v[182:183], v160 offset:0x2000
	ds_read_b64_tr_b16 v[184:185], v160 offset:0x3000
	s_waitcnt lgkmcnt(8)
	v_mfma_f32_16x16x32_bf16 v[94:97], v[232:235], v[106:109], v[94:97]
	v_mfma_f32_16x16x32_bf16 v[42:45], v[232:235], v[114:117], v[42:45]
	v_mfma_f32_16x16x32_bf16 v[90:93], v[240:243], v[106:109], v[90:93]
	v_mfma_f32_16x16x32_bf16 v[26:29], v[240:243], v[114:117], v[26:29]
	v_mfma_f32_16x16x32_bf16 v[94:97], v[236:239], v[110:113], v[94:97]
	v_mfma_f32_16x16x32_bf16 v[42:45], v[236:239], v[118:121], v[42:45]
	v_mfma_f32_16x16x32_bf16 v[90:93], v[244:247], v[110:113], v[90:93]
	v_mfma_f32_16x16x32_bf16 v[26:29], v[244:247], v[118:121], v[26:29]
	v_xor_b32_e32 v130, 0x80, v158
	ds_read_b64_tr_b16 v[232:233], v130 offset:0
	ds_read_b64_tr_b16 v[234:235], v130 offset:0x1000
	ds_read_b64_tr_b16 v[236:237], v130 offset:0x2000
	ds_read_b64_tr_b16 v[238:239], v130 offset:0x3000
	v_xor_b32_e32 v160, 0xa0, v158
	ds_read_b64_tr_b16 v[240:241], v160 offset:0
	ds_read_b64_tr_b16 v[242:243], v160 offset:0x1000
	ds_read_b64_tr_b16 v[244:245], v160 offset:0x2000
	ds_read_b64_tr_b16 v[246:247], v160 offset:0x3000
	s_waitcnt lgkmcnt(8)
	v_mfma_f32_16x16x32_bf16 v[86:89], v[170:173], v[106:109], v[86:89]
	v_mfma_f32_16x16x32_bf16 v[22:25], v[170:173], v[114:117], v[22:25]
	v_mfma_f32_16x16x32_bf16 v[82:85], v[178:181], v[106:109], v[82:85]
	v_mfma_f32_16x16x32_bf16 v[18:21], v[178:181], v[114:117], v[18:21]
	v_mfma_f32_16x16x32_bf16 v[86:89], v[174:177], v[110:113], v[86:89]
	v_mfma_f32_16x16x32_bf16 v[22:25], v[174:177], v[118:121], v[22:25]
	v_mfma_f32_16x16x32_bf16 v[82:85], v[182:185], v[110:113], v[82:85]
	v_mfma_f32_16x16x32_bf16 v[18:21], v[182:185], v[118:121], v[18:21]
	v_xor_b32_e32 v160, 0xc0, v158
	ds_read_b64_tr_b16 v[170:171], v160 offset:0
	ds_read_b64_tr_b16 v[172:173], v160 offset:0x1000
	ds_read_b64_tr_b16 v[174:175], v160 offset:0x2000
	ds_read_b64_tr_b16 v[176:177], v160 offset:0x3000
	v_xor_b32_e32 v158, 0xe0, v158
	ds_read_b64_tr_b16 v[178:179], v158 offset:0
	ds_read_b64_tr_b16 v[180:181], v158 offset:0x1000
	ds_read_b64_tr_b16 v[182:183], v158 offset:0x2000
	ds_read_b64_tr_b16 v[184:185], v158 offset:0x3000
	s_waitcnt lgkmcnt(8)
	v_mfma_f32_16x16x32_bf16 v[78:81], v[232:235], v[106:109], v[78:81]
	v_mfma_f32_16x16x32_bf16 v[14:17], v[232:235], v[114:117], v[14:17]
	v_mfma_f32_16x16x32_bf16 v[74:77], v[240:243], v[106:109], v[74:77]
	v_mfma_f32_16x16x32_bf16 v[2:5], v[240:243], v[114:117], v[2:5]
	v_mfma_f32_16x16x32_bf16 v[78:81], v[236:239], v[110:113], v[78:81]
	v_mfma_f32_16x16x32_bf16 v[14:17], v[236:239], v[118:121], v[14:17]
	v_mfma_f32_16x16x32_bf16 v[74:77], v[244:247], v[110:113], v[74:77]
	v_mfma_f32_16x16x32_bf16 v[2:5], v[244:247], v[118:121], v[2:5]
	s_waitcnt lgkmcnt(0)
	v_mfma_f32_16x16x32_bf16 v[70:73], v[170:173], v[106:109], v[70:73]
	v_mfma_f32_16x16x32_bf16 v[10:13], v[170:173], v[114:117], v[10:13]
	v_mfma_f32_16x16x32_bf16 v[66:69], v[178:181], v[106:109], v[66:69]
	v_mfma_f32_16x16x32_bf16 v[6:9], v[178:181], v[114:117], v[6:9]
	v_mfma_f32_16x16x32_bf16 v[70:73], v[174:177], v[110:113], v[70:73]
	v_mfma_f32_16x16x32_bf16 v[10:13], v[174:177], v[118:121], v[10:13]
	v_mfma_f32_16x16x32_bf16 v[66:69], v[182:185], v[110:113], v[66:69]
	v_mfma_f32_16x16x32_bf16 v[6:9], v[182:185], v[118:121], v[6:9]

.LBB0_420:
	v_add_u32_e32 v158, s67, v161
	v_add_u32_e32 v160, v158, v162
	ds_read_b128 v[170:173], v160 offset:0
	v_add_u32_e32 v169, v158, v163
	ds_read_b128 v[174:177], v169 offset:0
	v_add_u32_e32 v186, v158, v164
	ds_read_b128 v[178:181], v186 offset:0
	s_waitcnt lgkmcnt(2)
	v_add_u32_e32 v158, v158, v165
	v_mfma_f32_16x16x32_bf16 v[106:109], v[170:173], v[30:33], v[106:109]
	v_mfma_f32_16x16x32_bf16 v[110:113], v[170:173], v[50:53], v[110:113]
	ds_read_b128 v[170:173], v158 offset:0
	s_waitcnt lgkmcnt(2)
	v_mfma_f32_16x16x32_bf16 v[106:109], v[174:177], v[34:37], v[106:109]
	v_mfma_f32_16x16x32_bf16 v[110:113], v[174:177], v[54:57], v[110:113]
	ds_read_b128 v[174:177], v160 offset:0x1000
	s_waitcnt lgkmcnt(2)
	v_mfma_f32_16x16x32_bf16 v[106:109], v[178:181], v[38:41], v[106:109]
	ds_read_b128 v[182:185], v169 offset:0x1000
	s_waitcnt lgkmcnt(2)
	v_mfma_f32_16x16x32_bf16 v[178:181], v[178:181], v[58:61], v[110:113]
	v_mfma_f32_16x16x32_bf16 v[110:113], v[170:173], v[46:49], v[106:109]
	v_mfma_f32_16x16x32_bf16 v[106:109], v[170:173], v[62:65], v[178:181]
	ds_read_b128 v[170:173], v186 offset:0x1000
	s_waitcnt lgkmcnt(2)
	v_mfma_f32_16x16x32_bf16 v[114:117], v[174:177], v[30:33], v[114:117]
	v_mfma_f32_16x16x32_bf16 v[118:121], v[174:177], v[50:53], v[118:121]
	ds_read_b128 v[174:177], v158 offset:0x1000
	s_waitcnt lgkmcnt(2)
	v_mfma_f32_16x16x32_bf16 v[114:117], v[182:185], v[34:37], v[114:117]
	ds_read_b128 v[178:181], v160 offset:0x2000
	s_waitcnt lgkmcnt(2)
	v_mfma_f32_16x16x32_bf16 v[118:121], v[182:185], v[54:57], v[118:121]
	v_mfma_f32_16x16x32_bf16 v[114:117], v[170:173], v[38:41], v[114:117]
	ds_read_b128 v[182:185], v169 offset:0x2000
	s_waitcnt lgkmcnt(2)
	v_mfma_f32_16x16x32_bf16 v[170:173], v[170:173], v[58:61], v[118:121]
	v_mfma_f32_16x16x32_bf16 v[118:121], v[174:177], v[46:49], v[114:117]
	v_mfma_f32_16x16x32_bf16 v[114:117], v[174:177], v[62:65], v[170:173]
	ds_read_b128 v[170:173], v186 offset:0x2000
	s_waitcnt lgkmcnt(2)
	v_mfma_f32_16x16x32_bf16 v[122:125], v[178:181], v[30:33], v[122:125]
	ds_read_b128 v[174:177], v158 offset:0x2000
	s_waitcnt lgkmcnt(2)
	v_mfma_f32_16x16x32_bf16 v[130:133], v[178:181], v[50:53], v[130:133]
	v_mfma_f32_16x16x32_bf16 v[122:125], v[182:185], v[34:37], v[122:125]
	ds_read_b128 v[178:181], v160 offset:0x3000
	s_waitcnt lgkmcnt(2)
	v_mfma_f32_16x16x32_bf16 v[130:133], v[182:185], v[54:57], v[130:133]
	s_nop 1
	v_mfma_f32_16x16x32_bf16 v[122:125], v[170:173], v[38:41], v[122:125]
	ds_read_b128 v[182:185], v169 offset:0x3000
	s_waitcnt lgkmcnt(2)
	v_mfma_f32_16x16x32_bf16 v[170:173], v[170:173], v[58:61], v[130:133]
	v_mfma_f32_16x16x32_bf16 v[130:133], v[174:177], v[46:49], v[122:125]
	v_mfma_f32_16x16x32_bf16 v[122:125], v[174:177], v[62:65], v[170:173]
	ds_read_b128 v[170:173], v186 offset:0x3000
	s_waitcnt lgkmcnt(2)
	v_mfma_f32_16x16x32_bf16 v[126:129], v[178:181], v[30:33], v[126:129]
	ds_read_b128 v[174:177], v158 offset:0x3000
	s_waitcnt lgkmcnt(2)
	v_mfma_f32_16x16x32_bf16 v[134:137], v[178:181], v[50:53], v[134:137]
	v_mfma_f32_16x16x32_bf16 v[126:129], v[182:185], v[34:37], v[126:129]
	s_waitcnt lgkmcnt(1)
	v_mfma_f32_16x16x32_bf16 v[134:137], v[182:185], v[54:57], v[134:137]
	s_nop 1
	v_mfma_f32_16x16x32_bf16 v[126:129], v[170:173], v[38:41], v[126:129]
	s_waitcnt lgkmcnt(0)
	v_mfma_f32_16x16x32_bf16 v[170:173], v[170:173], v[58:61], v[134:137]
	v_and_b32_e32 v160, 64, v208
	v_xor_b32_e32 v158, 16, v208
	v_add_u32_e32 v160, 64, v160
	v_cmp_lt_i32_e32 vcc, v158, v160
	v_mfma_f32_16x16x32_bf16 v[134:137], v[174:177], v[46:49], v[126:129]
	s_mov_b64 s[48:49], 0
	v_cndmask_b32_e32 v158, v208, v158, vcc
	v_lshlrev_b32_e32 v169, 2, v158
	v_xor_b32_e32 v158, 32, v208
	v_cmp_lt_i32_e32 vcc, v158, v160
	v_mfma_f32_16x16x32_bf16 v[126:129], v[174:177], v[62:65], v[170:173]
	s_mov_b64 s[52:53], 0
	v_cndmask_b32_e32 v158, v208, v158, vcc
	s_nop 0
	v_lshlrev_b32_e32 v170, 2, v158
	v_max3_f32 v158, v110, s30, v111
	v_max3_f32 v158, v158, v112, v113
	v_max3_f32 v158, v158, v118, v119
	v_max3_f32 v158, v158, v120, v121
	v_max3_f32 v158, v158, v130, v131
	v_max3_f32 v158, v158, v132, v133
	v_max3_f32 v158, v158, v134, v135
	v_max3_f32 v158, v158, v136, v137
	v_max3_f32 v160, v106, s30, v107
	v_max3_f32 v160, v160, v108, v109
	v_max3_f32 v160, v160, v114, v115
	v_max3_f32 v160, v160, v116, v117
	v_max3_f32 v160, v160, v122, v123
	v_max3_f32 v160, v160, v124, v125
	v_max3_f32 v160, v160, v126, v127
	v_max3_f32 v160, v160, v128, v129
	v_mov_b32_e32 v230, v158
	v_mov_b32_e32 v231, v160
	s_nop 1
	v_permlane16_swap_b32 v230, v158
	v_permlane16_swap_b32 v231, v160
	v_max_f32_e32 v158, v158, v230
	v_max_f32_e32 v160, v160, v231
	v_mov_b32_e32 v230, v158
	v_mov_b32_e32 v231, v160
	s_nop 1
	v_permlane32_swap_b32 v230, v158
	v_permlane32_swap_b32 v231, v160
	v_max_f32_e32 v158, v158, v230
	v_max_f32_e32 v160, v160, v231
	v_cmp_lt_f32_e64 s[54:55], s31, v158
	v_cmp_lt_f32_e32 vcc, s34, v158
	s_orn2_b64 s[52:53], vcc, s[46:47]
	s_and_b64 s[52:53], s[52:53], s[54:55]
	v_cmp_lt_f32_e64 s[54:55], s31, v160
	v_cmp_lt_f32_e32 vcc, s34, v160
	s_orn2_b64 s[48:49], vcc, s[44:45]
	s_and_b64 s[48:49], s[48:49], s[54:55]
	s_or_b64 s[54:55], s[52:53], s[48:49]
	s_cbranch_scc0 .LBB0_413
	v_cndmask_b32_e64 v160, 0, v160, s[48:49]
	v_cndmask_b32_e64 v158, 0, v158, s[52:53]
	v_exp_f32_e64 v170, -v160
	v_exp_f32_e64 v169, -v158
	s_and_b64 vcc, s[48:49], s[44:45]
	s_or_b64 s[48:49], s[44:45], s[48:49]
	v_cndmask_b32_e32 v171, 1.0, v170, vcc
	s_and_b64 vcc, s[52:53], s[46:47]
	s_or_b64 s[52:53], s[46:47], s[52:53]
	v_add_f32_e32 v167, v167, v158
	v_sub_f32_e32 v110, v110, v158
	v_sub_f32_e32 v111, v111, v158
	v_sub_f32_e32 v112, v112, v158
	v_sub_f32_e32 v113, v113, v158
	v_sub_f32_e32 v118, v118, v158
	v_sub_f32_e32 v119, v119, v158
	v_sub_f32_e32 v120, v120, v158
	v_sub_f32_e32 v121, v121, v158
	v_sub_f32_e32 v130, v130, v158
	v_sub_f32_e32 v131, v131, v158
	v_sub_f32_e32 v132, v132, v158
	v_sub_f32_e32 v133, v133, v158
	v_sub_f32_e32 v134, v134, v158
	v_sub_f32_e32 v135, v135, v158
	v_sub_f32_e32 v136, v136, v158
	v_sub_f32_e32 v137, v137, v158
	v_cndmask_b32_e32 v170, 1.0, v169, vcc
	v_mov_b32_e32 v158, v171
	s_andn2_b64 s[46:47], s[46:47], exec
	s_and_b64 s[52:53], s[52:53], exec
	s_andn2_b64 s[44:45], s[44:45], exec
	s_and_b64 s[48:49], s[48:49], exec
	v_pk_mul_f32 v[96:97], v[96:97], v[170:171] op_sel_hi:[1,0]
	v_pk_mul_f32 v[94:95], v[94:95], v[170:171] op_sel_hi:[1,0]
	v_pk_mul_f32 v[92:93], v[92:93], v[170:171] op_sel_hi:[1,0]
	v_pk_mul_f32 v[90:91], v[90:91], v[170:171] op_sel_hi:[1,0]
	v_pk_mul_f32 v[88:89], v[88:89], v[170:171] op_sel_hi:[1,0]
	v_pk_mul_f32 v[86:87], v[86:87], v[170:171] op_sel_hi:[1,0]
	v_pk_mul_f32 v[84:85], v[84:85], v[170:171] op_sel_hi:[1,0]
	v_pk_mul_f32 v[82:83], v[82:83], v[170:171] op_sel_hi:[1,0]
	v_pk_mul_f32 v[80:81], v[80:81], v[170:171] op_sel_hi:[1,0]
	v_pk_mul_f32 v[78:79], v[78:79], v[170:171] op_sel_hi:[1,0]
	v_pk_mul_f32 v[76:77], v[76:77], v[170:171] op_sel_hi:[1,0]
	v_pk_mul_f32 v[74:75], v[74:75], v[170:171] op_sel_hi:[1,0]
	v_pk_mul_f32 v[72:73], v[72:73], v[170:171] op_sel_hi:[1,0]
	v_pk_mul_f32 v[70:71], v[70:71], v[170:171] op_sel_hi:[1,0]
	v_pk_mul_f32 v[68:69], v[68:69], v[170:171] op_sel_hi:[1,0]
	v_pk_mul_f32 v[66:67], v[66:67], v[170:171] op_sel_hi:[1,0]
	v_add_f32_e32 v168, v168, v160
	v_pk_mul_f32 v[144:145], v[144:145], v[170:171]
	v_pk_mul_f32 v[44:45], v[44:45], v[158:159] op_sel_hi:[1,0]
	v_pk_mul_f32 v[42:43], v[42:43], v[158:159] op_sel_hi:[1,0]
	v_pk_mul_f32 v[28:29], v[28:29], v[158:159] op_sel_hi:[1,0]
	v_pk_mul_f32 v[26:27], v[26:27], v[158:159] op_sel_hi:[1,0]
	v_pk_mul_f32 v[24:25], v[24:25], v[158:159] op_sel_hi:[1,0]
	v_pk_mul_f32 v[22:23], v[22:23], v[158:159] op_sel_hi:[1,0]
	v_pk_mul_f32 v[20:21], v[20:21], v[158:159] op_sel_hi:[1,0]
	v_pk_mul_f32 v[18:19], v[18:19], v[158:159] op_sel_hi:[1,0]
	v_pk_mul_f32 v[16:17], v[16:17], v[158:159] op_sel_hi:[1,0]
	v_pk_mul_f32 v[14:15], v[14:15], v[158:159] op_sel_hi:[1,0]
	v_pk_mul_f32 v[4:5], v[4:5], v[158:159] op_sel_hi:[1,0]
	v_pk_mul_f32 v[2:3], v[2:3], v[158:159] op_sel_hi:[1,0]
	v_pk_mul_f32 v[12:13], v[12:13], v[158:159] op_sel_hi:[1,0]
	v_pk_mul_f32 v[10:11], v[10:11], v[158:159] op_sel_hi:[1,0]
	v_pk_mul_f32 v[8:9], v[8:9], v[158:159] op_sel_hi:[1,0]
	v_pk_mul_f32 v[6:7], v[6:7], v[158:159] op_sel_hi:[1,0]
	v_sub_f32_e32 v106, v106, v160
	v_sub_f32_e32 v107, v107, v160
	v_sub_f32_e32 v108, v108, v160
	v_sub_f32_e32 v109, v109, v160
	v_sub_f32_e32 v114, v114, v160
	v_sub_f32_e32 v115, v115, v160
	v_sub_f32_e32 v116, v116, v160
	v_sub_f32_e32 v117, v117, v160
	v_sub_f32_e32 v122, v122, v160
	v_sub_f32_e32 v123, v123, v160
	v_sub_f32_e32 v124, v124, v160
	v_sub_f32_e32 v125, v125, v160
	v_sub_f32_e32 v126, v126, v160
	v_sub_f32_e32 v127, v127, v160
	v_sub_f32_e32 v128, v128, v160
	v_sub_f32_e32 v129, v129, v160
	s_or_b64 s[46:47], s[46:47], s[52:53]
	s_or_b64 s[44:45], s[44:45], s[48:49]
	s_branch .LBB0_413
